# v87 + grid barriers: 16th and 28th local arriver issue an extra early L2 write-back so the last arriver's release write-back finds fewer dirty lines
# speedup vs baseline: 1.0016x; 1.0016x over previous
.LBB0_42:
	s_or_b64 exec, exec, s[6:7]
	v_cvt_f32_u32_e32 v4, v2
	s_waitcnt vmcnt(0)
	v_readfirstlane_b32 s4, v3
	v_sub_u32_e32 v3, 0, v2
	v_rcp_iflag_f32_e32 v4, v4
	v_add_u32_e32 v5, s4, v1
	v_mul_f32_e32 v4, 0x4f7ffffe, v4
	v_cvt_u32_f32_e32 v4, v4
	v_mul_lo_u32 v1, v3, v4
	v_mul_hi_u32 v1, v4, v1
	v_add_u32_e32 v1, v4, v1
	v_mul_hi_u32 v1, v5, v1
	v_mul_lo_u32 v3, v1, v2
	v_sub_u32_e32 v3, v5, v3
	v_add_u32_e32 v4, 1, v1
	v_cmp_ge_u32_e32 vcc, v3, v2
	s_nop 1
	v_cndmask_b32_e32 v1, v1, v4, vcc
	v_sub_u32_e32 v4, v3, v2
	v_cndmask_b32_e32 v3, v3, v4, vcc
	v_add_u32_e32 v4, 1, v1
	v_cmp_ge_u32_e32 vcc, v3, v2
	v_add_u32_e32 v3, 1, v5
	s_nop 0
	v_cndmask_b32_e32 v1, v1, v4, vcc
	v_mul_lo_u32 v4, v2, v1
	v_add_u32_e32 v2, v4, v2
	v_sub_u32_e32 v4, v2, v3
	v_cmp_eq_u32_e32 vcc, 16, v4
	v_cmp_eq_u32_e64 s[4:5], 4, v4
	s_or_b64 vcc, vcc, s[4:5]
	s_cbranch_vccz .Lopt26_1
	buffer_wbl2 sc1
.Lopt26_1:
	v_cmp_ne_u32_e32 vcc, v3, v2
	s_and_saveexec_b64 s[4:5], vcc
	s_xor_b64 s[4:5], exec, s[4:5]
	s_cbranch_execz .LBB0_56
	s_waitcnt lgkmcnt(0)
	v_mov_b32_e32 v0, 0x2000
	global_load_dword v0, v0, s[2:3] offset:1024 sc1
	s_add_u32 s10, s2, 0x2400
	s_addc_u32 s11, s3, 0
	s_waitcnt vmcnt(0)
	v_cmp_eq_u32_e32 vcc, v0, v1
	s_and_saveexec_b64 s[6:7], vcc
	s_cbranch_execz .LBB0_55
	s_mov_b32 s33, 1
	s_mov_b64 s[12:13], 0
	v_mov_b32_e32 v0, 0
	s_branch .LBB0_46

.LBB0_192:
	s_or_b64 exec, exec, s[10:11]
	v_cvt_f32_u32_e32 v4, v2
	s_waitcnt vmcnt(0)
	v_readfirstlane_b32 s4, v3
	v_sub_u32_e32 v3, 0, v2
	v_rcp_iflag_f32_e32 v4, v4
	v_add_u32_e32 v5, s4, v1
	v_mul_f32_e32 v4, 0x4f7ffffe, v4
	v_cvt_u32_f32_e32 v4, v4
	v_mul_lo_u32 v1, v3, v4
	v_mul_hi_u32 v1, v4, v1
	v_add_u32_e32 v1, v4, v1
	v_mul_hi_u32 v1, v5, v1
	v_mul_lo_u32 v3, v1, v2
	v_sub_u32_e32 v3, v5, v3
	v_add_u32_e32 v4, 1, v1
	v_cmp_ge_u32_e32 vcc, v3, v2
	s_nop 1
	v_cndmask_b32_e32 v1, v1, v4, vcc
	v_sub_u32_e32 v4, v3, v2
	v_cndmask_b32_e32 v3, v3, v4, vcc
	v_add_u32_e32 v4, 1, v1
	v_cmp_ge_u32_e32 vcc, v3, v2
	v_add_u32_e32 v3, 1, v5
	s_nop 0
	v_cndmask_b32_e32 v1, v1, v4, vcc
	v_mul_lo_u32 v4, v2, v1
	v_add_u32_e32 v2, v4, v2
	v_sub_u32_e32 v4, v2, v3
	v_cmp_eq_u32_e32 vcc, 16, v4
	v_cmp_eq_u32_e64 s[4:5], 4, v4
	s_or_b64 vcc, vcc, s[4:5]
	s_cbranch_vccz .Lopt26_2
	buffer_wbl2 sc1
.Lopt26_2:
	v_cmp_ne_u32_e32 vcc, v3, v2
	s_and_saveexec_b64 s[4:5], vcc
	s_xor_b64 s[4:5], exec, s[4:5]
	s_cbranch_execz .LBB0_206
	s_waitcnt lgkmcnt(0)
	v_mov_b32_e32 v0, 0x2000
	global_load_dword v0, v0, s[2:3] offset:1024 sc1
	s_add_u32 s12, s2, 0x2400
	s_addc_u32 s13, s3, 0
	s_waitcnt vmcnt(0)
	v_cmp_eq_u32_e32 vcc, v0, v1
	s_and_saveexec_b64 s[10:11], vcc
	s_cbranch_execz .LBB0_205
	s_mov_b32 s26, 1
	s_mov_b64 s[14:15], 0
	v_mov_b32_e32 v0, 0
	s_branch .LBB0_196

.Lopt26_3:
	v_cmp_ne_u32_e32 vcc, v3, v2
	s_and_saveexec_b64 s[4:5], vcc
	s_xor_b64 s[4:5], exec, s[4:5]
	s_cbranch_execz .LBB0_301
	s_waitcnt lgkmcnt(0)
	v_mov_b32_e32 v0, 0x2000
	global_load_dword v0, v0, s[2:3] offset:1024 sc1
	s_add_u32 s12, s2, 0x2400
	s_addc_u32 s13, s3, 0
	s_waitcnt vmcnt(0)
	v_cmp_eq_u32_e32 vcc, v0, v1
	s_and_saveexec_b64 s[10:11], vcc
	s_cbranch_execz .LBB0_300
	s_mov_b32 s24, 1
	s_mov_b64 s[14:15], 0
	v_mov_b32_e32 v0, 0
	s_branch .LBB0_291

.LBB0_485:
	s_or_b64 exec, exec, s[8:9]
	v_cvt_f32_u32_e32 v4, v2
	s_waitcnt vmcnt(0)
	v_readfirstlane_b32 s4, v3
	v_sub_u32_e32 v3, 0, v2
	v_rcp_iflag_f32_e32 v4, v4
	v_add_u32_e32 v5, s4, v1
	v_mul_f32_e32 v4, 0x4f7ffffe, v4
	v_cvt_u32_f32_e32 v4, v4
	v_mul_lo_u32 v1, v3, v4
	v_mul_hi_u32 v1, v4, v1
	v_add_u32_e32 v1, v4, v1
	v_mul_hi_u32 v1, v5, v1
	v_mul_lo_u32 v3, v1, v2
	v_sub_u32_e32 v3, v5, v3
	v_add_u32_e32 v4, 1, v1
	v_cmp_ge_u32_e32 vcc, v3, v2
	s_nop 1
	v_cndmask_b32_e32 v1, v1, v4, vcc
	v_sub_u32_e32 v4, v3, v2
	v_cndmask_b32_e32 v3, v3, v4, vcc
	v_add_u32_e32 v4, 1, v1
	v_cmp_ge_u32_e32 vcc, v3, v2
	v_add_u32_e32 v3, 1, v5
	s_nop 0
	v_cndmask_b32_e32 v1, v1, v4, vcc
	v_mul_lo_u32 v4, v2, v1
	v_add_u32_e32 v2, v4, v2
	v_sub_u32_e32 v4, v2, v3
	v_cmp_eq_u32_e32 vcc, 16, v4
	v_cmp_eq_u32_e64 s[4:5], 4, v4
	s_or_b64 vcc, vcc, s[4:5]
	s_cbranch_vccz .Lopt26_5
	buffer_wbl2 sc1
.Lopt26_5:
	v_cmp_ne_u32_e32 vcc, v3, v2
	s_and_saveexec_b64 s[4:5], vcc
	s_xor_b64 s[4:5], exec, s[4:5]
	s_cbranch_execz .LBB0_499
	s_waitcnt lgkmcnt(0)
	v_mov_b32_e32 v0, 0x2000
	global_load_dword v0, v0, s[2:3] offset:1024 sc1
	s_add_u32 s10, s2, 0x2400
	s_addc_u32 s11, s3, 0
	s_waitcnt vmcnt(0)
	v_cmp_eq_u32_e32 vcc, v0, v1
	s_and_saveexec_b64 s[8:9], vcc
	s_cbranch_execz .LBB0_498
	s_mov_b32 s22, 1
	s_mov_b64 s[12:13], 0
	v_mov_b32_e32 v0, 0
	s_branch .LBB0_489

.Lopt26_6:
	v_cmp_ne_u32_e32 vcc, v3, v2
	s_and_saveexec_b64 s[4:5], vcc
	s_xor_b64 s[4:5], exec, s[4:5]
	s_cbranch_execz .LBB0_558
	s_waitcnt lgkmcnt(0)
	v_mov_b32_e32 v0, 0x2000
	global_load_dword v0, v0, s[2:3] offset:1024 sc1
	s_add_u32 s8, s2, 0x2400
	s_addc_u32 s9, s3, 0
	s_waitcnt vmcnt(0)
	v_cmp_eq_u32_e32 vcc, v0, v1
	s_and_saveexec_b64 s[6:7], vcc
	s_cbranch_execz .LBB0_557
	s_mov_b32 s20, 1
	s_mov_b64 s[10:11], 0
	v_mov_b32_e32 v0, 0
	s_branch .LBB0_548
